# baseline (speedup 1.0000x reference)
_ZN12_GLOBAL__N_14k_fcEPKtPKiS1_PKfS5_Pf:
	s_load_dwordx8 s[4:11], s[0:1], 0x0
	s_load_dwordx4 s[12:15], s[0:1], 0x20
	s_and_b32 s3, s2, 7
	s_lshr_b32 s20, s2, 3
	s_lshr_b32 s19, s20, 2
	s_lshl_b32 s3, s3, 3
	s_add_u32 s19, s19, s3
	s_and_b32 s20, s20, 3
	v_lshrrev_b32_e32 v1, 6, v0
	v_and_b32_e32 v12, 63, v0
	v_and_b32_e32 v13, 15, v0
	v_readfirstlane_b32 s16, v1
	v_lshrrev_b32_e32 v14, 4, v12
	s_nop 3
	s_lshr_b32 s17, s16, 2
	s_and_b32 s18, s16, 3
	v_lshrrev_b32_e32 v70, 2, v12
	s_lshl_b32 s90, s19, 8
	s_lshl_b32 s91, s16, 5
	s_add_u32 s90, s90, s91
	v_add_u32_e32 v73, s90, v70
	v_add_u32_e32 v74, 16, v73
	s_waitcnt lgkmcnt(0)
	v_lshlrev_b32_e32 v75, 3, v73
	v_lshlrev_b32_e32 v76, 3, v74
	global_load_dwordx2 v[64:65], v75, s[6:7]
	global_load_dwordx2 v[66:67], v76, s[6:7]
	s_mul_i32 s90, s20, 0x180
	s_mul_i32 s91, s18, 96
	s_add_u32 s90, s90, s91
	v_lshl_add_u32 v15, v14, 2, s90
	v_lshlrev_b32_e32 v15, 2, v15
	global_load_dwordx4 v[16:19], v15, s[10:11] offset:0
	global_load_dwordx4 v[20:23], v15, s[10:11] offset:64
	global_load_dwordx4 v[24:27], v15, s[10:11] offset:128
	global_load_dwordx4 v[28:31], v15, s[10:11] offset:192
	global_load_dwordx4 v[32:35], v15, s[10:11] offset:256
	global_load_dwordx4 v[36:39], v15, s[10:11] offset:320
	v_mul_u32_u24_e32 v77, 0x1800, v13
	v_add_u32_e32 v77, v77, v15
	v_mov_b32_e32 v40, 0
	v_mov_b32_e32 v41, 0
	v_mov_b32_e32 v42, 0
	v_mov_b32_e32 v43, 0
	v_mov_b32_e32 v44, 0
	v_mov_b32_e32 v45, 0
	v_mov_b32_e32 v46, 0
	v_mov_b32_e32 v47, 0
	v_mov_b32_e32 v48, 0
	v_mov_b32_e32 v49, 0
	v_mov_b32_e32 v50, 0
	v_mov_b32_e32 v51, 0
	v_mov_b32_e32 v52, 0
	v_mov_b32_e32 v53, 0
	v_mov_b32_e32 v54, 0
	v_mov_b32_e32 v55, 0
	v_mov_b32_e32 v56, 0
	v_mov_b32_e32 v57, 0
	v_mov_b32_e32 v58, 0
	v_mov_b32_e32 v59, 0
	v_mov_b32_e32 v60, 0
	v_mov_b32_e32 v61, 0
	v_mov_b32_e32 v62, 0
	v_mov_b32_e32 v63, 0
	s_mov_b32 exec_lo, 0xff00ff
	s_mov_b32 exec_hi, 0xff00ff
	global_load_dwordx4 v[40:43], v77, s[12:13] offset:0
	global_load_dwordx4 v[44:47], v77, s[12:13] offset:64
	global_load_dwordx4 v[48:51], v77, s[12:13] offset:128
	global_load_dwordx4 v[52:55], v77, s[12:13] offset:192
	global_load_dwordx4 v[56:59], v77, s[12:13] offset:256
	global_load_dwordx4 v[60:63], v77, s[12:13] offset:320
	s_mov_b64 exec, -1
	v_lshlrev_b32_e32 v15, 6, v13
	v_lshl_add_u32 v15, v14, 4, v15
	v_lshrrev_b32_e32 v78, 3, v13
	v_lshlrev_b32_e32 v78, 5, v78
	v_xor_b32_e32 v15, v15, v78
	s_lshl_b32 s90, s17, 13
	v_add_u32_e32 v1, s90, v15
	v_add_u32_e32 v2, 0x14000, v1
	s_mul_i32 s90, s18, 0x1800
	s_add_u32 s90, s90, 0x4000
	v_add_u32_e32 v3, s90, v15
	v_add_u32_e32 v4, 0x14000, v3
	v_and_b32_e32 v71, 3, v12
	v_lshrrev_b32_e32 v72, 5, v12
	v_lshlrev_b32_e32 v72, 1, v72
	v_xor_b32_e32 v71, v71, v72
	v_lshlrev_b32_e32 v71, 4, v71
	v_lshl_add_u32 v11, v70, 6, v71
	s_mul_i32 s90, s20, 0x180
	s_mul_i32 s91, s16, 48
	s_add_u32 s90, s90, s91
	s_lshl_b32 s90, s90, 6
	s_add_u32 s28, s8, s90
	s_addc_u32 s29, s9, 0
	s_add_u32 s30, s28, 0x18000
	s_addc_u32 s31, s29, 0
	s_add_u32 s32, s28, 0x400
	s_addc_u32 s33, s29, 0
	s_add_u32 s34, s32, 0x18000
	s_addc_u32 s35, s33, 0
	s_add_u32 s36, s28, 0x800
	s_addc_u32 s37, s29, 0
	s_add_u32 s38, s36, 0x18000
	s_addc_u32 s39, s37, 0
	s_mov_b64 s[24:25], s[4:5]
	s_add_u32 s26, s4, 0x40
	s_addc_u32 s27, s5, 0
	s_add_u32 s96, s4, 0x1000000
	s_addc_u32 s97, s5, 0
	s_lshl_b32 s22, s16, 11
	s_mul_i32 s23, s16, 0xc00
	s_add_u32 s23, s23, 0x4000
	s_mov_b32 s21, 0
	s_lshr_b32 s92, s19, 1
	s_lshl_b32 s92, s92, 9
	s_movk_i32 s93, 0x1ff
	s_movk_i32 s94, 0x200
	v_lshl_add_u32 v5, v73, 10, v71
	v_lshl_add_u32 v6, v74, 10, v71
	s_add_u32 s24, s24, 0x1000000
	s_addc_u32 s25, s25, 0
	s_add_u32 s26, s26, 0x1000000
	s_addc_u32 s27, s27, 0
	s_add_u32 s28, s28, 0x180000
	s_addc_u32 s29, s29, 0
	s_add_u32 s30, s30, 0x180000
	s_addc_u32 s31, s31, 0
	s_add_u32 s32, s32, 0x180000
	s_addc_u32 s33, s33, 0
	s_add_u32 s34, s34, 0x180000
	s_addc_u32 s35, s35, 0
	s_add_u32 s36, s36, 0x180000
	s_addc_u32 s37, s37, 0
	s_add_u32 s38, s38, 0x180000
	s_addc_u32 s39, s39, 0
	s_cmp_lg_u32 s17, 0
	s_cbranch_scc1 .Lfc_h1_entry
	s_add_u32 m0, s22, 0x0
	s_nop 0
	global_load_lds_dwordx4 v5, s[24:25]
	s_add_u32 m0, s22, 0x400
	s_nop 0
	global_load_lds_dwordx4 v6, s[24:25]
	s_add_u32 m0, s23, 0x0
	s_nop 0
	global_load_lds_dwordx4 v11, s[28:29]
	s_add_u32 m0, s23, 0x400
	s_nop 0
	global_load_lds_dwordx4 v11, s[32:33]
	s_add_u32 m0, s23, 0x800
	s_nop 0
	global_load_lds_dwordx4 v11, s[36:37]
	s_add_u32 s24, s24, 0x80
	s_addc_u32 s25, s25, 0
	s_add_u32 s28, s28, 0x30000
	s_addc_u32 s29, s29, 0
	s_add_u32 s32, s32, 0x30000
	s_addc_u32 s33, s33, 0
	s_add_u32 s36, s36, 0x30000
	s_addc_u32 s37, s37, 0
	s_add_u32 m0, s22, 0xa000
	s_nop 0
	global_load_lds_dwordx4 v5, s[26:27]
	s_add_u32 m0, s22, 0xa400
	s_nop 0
	global_load_lds_dwordx4 v6, s[26:27]
	s_add_u32 m0, s23, 0xa000
	s_nop 0
	global_load_lds_dwordx4 v11, s[30:31]
	s_add_u32 m0, s23, 0xa400
	s_nop 0
	global_load_lds_dwordx4 v11, s[34:35]
	s_add_u32 m0, s23, 0xa800
	s_nop 0
	global_load_lds_dwordx4 v11, s[38:39]
	s_add_u32 s26, s26, 0x80
	s_addc_u32 s27, s27, 0
	s_add_u32 s30, s30, 0x30000
	s_addc_u32 s31, s31, 0
	s_add_u32 s34, s34, 0x30000
	s_addc_u32 s35, s35, 0
	s_add_u32 s38, s38, 0x30000
	s_addc_u32 s39, s39, 0
	s_add_u32 m0, s22, 0x14000
	s_nop 0
	global_load_lds_dwordx4 v5, s[24:25]
	s_add_u32 m0, s22, 0x14400
	s_nop 0
	global_load_lds_dwordx4 v6, s[24:25]
	s_add_u32 m0, s23, 0x14000
	s_nop 0
	global_load_lds_dwordx4 v11, s[28:29]
	s_add_u32 m0, s23, 0x14400
	s_nop 0
	global_load_lds_dwordx4 v11, s[32:33]
	s_add_u32 m0, s23, 0x14800
	s_nop 0
	global_load_lds_dwordx4 v11, s[36:37]
	s_add_u32 s24, s24, 0x80
	s_addc_u32 s25, s25, 0
	s_add_u32 s28, s28, 0x30000
	s_addc_u32 s29, s29, 0
	s_add_u32 s32, s32, 0x30000
	s_addc_u32 s33, s33, 0
	s_add_u32 s36, s36, 0x30000
	s_addc_u32 s37, s37, 0
	s_add_u32 m0, s22, 0x1e000
	s_nop 0
	global_load_lds_dwordx4 v5, s[26:27]
	s_add_u32 m0, s22, 0x1e400
	s_nop 0
	global_load_lds_dwordx4 v6, s[26:27]
	s_add_u32 m0, s23, 0x1e000
	s_nop 0
	global_load_lds_dwordx4 v11, s[30:31]
	s_add_u32 m0, s23, 0x1e400
	s_nop 0
	global_load_lds_dwordx4 v11, s[34:35]
	s_add_u32 m0, s23, 0x1e800
	s_nop 0
	global_load_lds_dwordx4 v11, s[38:39]
	s_add_u32 s26, s26, 0x80
	s_addc_u32 s27, s27, 0
	s_add_u32 s30, s30, 0x30000
	s_addc_u32 s31, s31, 0
	s_add_u32 s34, s34, 0x30000
	s_addc_u32 s35, s35, 0
	s_add_u32 s38, s38, 0x30000
	s_addc_u32 s39, s39, 0
	s_waitcnt vmcnt(20)
	v_med3_i32 v64, v64, 0, s93
	v_med3_i32 v65, v65, 1, s94
	v_med3_i32 v66, v66, 0, s93
	v_med3_i32 v67, v67, 1, s94
	v_add_u32_e32 v64, s92, v64
	v_add_u32_e32 v66, s92, v66
	v_add_u32_e32 v65, s92, v65
	v_add_u32_e32 v67, s92, v67
	v_add_u32_e32 v65, -1, v65
	v_add_u32_e32 v67, -1, v67
	v_lshl_add_u32 v7, v64, 10, v71
	v_lshl_add_u32 v8, v66, 10, v71
	v_lshl_add_u32 v9, v65, 10, v71
	v_lshl_add_u32 v10, v67, 10, v71
	v_cvt_pk_f16_f32 v12, v40, v41
	v_cvt_pk_f16_f32 v13, v42, v43
	v_cvt_pk_f16_f32 v14, v44, v45
	v_cvt_pk_f16_f32 v15, v46, v47
	v_cvt_pk_f16_f32 v56, v56, v57
	v_cvt_pk_f16_f32 v57, v58, v59
	v_cvt_pk_f16_f32 v58, v60, v61
	v_cvt_pk_f16_f32 v59, v62, v63
	v_cvt_pk_f16_f32 v60, v48, v49
	v_cvt_pk_f16_f32 v61, v50, v51
	v_cvt_pk_f16_f32 v62, v52, v53
	v_cvt_pk_f16_f32 v63, v54, v55
	v_mov_b32_e32 v64, v16
	v_mov_b32_e32 v65, v17
	v_mov_b32_e32 v66, v18
	v_mov_b32_e32 v67, v19
	v_mov_b32_e32 v68, v20
	v_mov_b32_e32 v69, v21
	v_mov_b32_e32 v70, v22
	v_mov_b32_e32 v71, v23
	v_mov_b32_e32 v72, v24
	v_mov_b32_e32 v73, v25
	v_mov_b32_e32 v74, v26
	v_mov_b32_e32 v75, v27
	v_mov_b32_e32 v76, v28
	v_mov_b32_e32 v77, v29
	v_mov_b32_e32 v78, v30
	v_mov_b32_e32 v79, v31
	v_mov_b32_e32 v80, v32
	v_mov_b32_e32 v81, v33
	v_mov_b32_e32 v82, v34
	v_mov_b32_e32 v83, v35
	v_mov_b32_e32 v84, v36
	v_mov_b32_e32 v85, v37
	v_mov_b32_e32 v86, v38
	v_mov_b32_e32 v87, v39
	v_mov_b32_e32 v88, v16
	v_mov_b32_e32 v89, v17
	v_mov_b32_e32 v90, v18
	v_mov_b32_e32 v91, v19
	v_mov_b32_e32 v92, v20
	v_mov_b32_e32 v93, v21
	v_mov_b32_e32 v94, v22
	v_mov_b32_e32 v95, v23
	v_mov_b32_e32 v96, v24
	v_mov_b32_e32 v97, v25
	v_mov_b32_e32 v98, v26
	v_mov_b32_e32 v99, v27
	v_mov_b32_e32 v100, v28
	v_mov_b32_e32 v101, v29
	v_mov_b32_e32 v102, v30
	v_mov_b32_e32 v103, v31
	v_mov_b32_e32 v104, v32
	v_mov_b32_e32 v105, v33
	v_mov_b32_e32 v106, v34
	v_mov_b32_e32 v107, v35
	v_mov_b32_e32 v108, v36
	v_mov_b32_e32 v109, v37
	v_mov_b32_e32 v110, v38
	v_mov_b32_e32 v111, v39
	v_mov_b32_e32 v112, v16
	v_mov_b32_e32 v113, v17
	v_mov_b32_e32 v114, v18
	v_mov_b32_e32 v115, v19
	v_mov_b32_e32 v116, v20
	v_mov_b32_e32 v117, v21
	v_mov_b32_e32 v118, v22
	v_mov_b32_e32 v119, v23
	v_mov_b32_e32 v120, v24
	v_mov_b32_e32 v121, v25
	v_mov_b32_e32 v122, v26
	v_mov_b32_e32 v123, v27
	v_mov_b32_e32 v124, v28
	v_mov_b32_e32 v125, v29
	v_mov_b32_e32 v126, v30
	v_mov_b32_e32 v127, v31
	v_mov_b32_e32 v128, v32
	v_mov_b32_e32 v129, v33
	v_mov_b32_e32 v130, v34
	v_mov_b32_e32 v131, v35
	v_mov_b32_e32 v132, v36
	v_mov_b32_e32 v133, v37
	v_mov_b32_e32 v134, v38
	v_mov_b32_e32 v135, v39
	v_mov_b32_e32 v136, v16
	v_mov_b32_e32 v137, v17
	v_mov_b32_e32 v138, v18
	v_mov_b32_e32 v139, v19
	v_mov_b32_e32 v140, v20
	v_mov_b32_e32 v141, v21
	v_mov_b32_e32 v142, v22
	v_mov_b32_e32 v143, v23
	v_mov_b32_e32 v144, v24
	v_mov_b32_e32 v145, v25
	v_mov_b32_e32 v146, v26
	v_mov_b32_e32 v147, v27
	v_mov_b32_e32 v148, v28
	v_mov_b32_e32 v149, v29
	v_mov_b32_e32 v150, v30
	v_mov_b32_e32 v151, v31
	v_mov_b32_e32 v152, v32
	v_mov_b32_e32 v153, v33
	v_mov_b32_e32 v154, v34
	v_mov_b32_e32 v155, v35
	v_mov_b32_e32 v156, v36
	v_mov_b32_e32 v157, v37
	v_mov_b32_e32 v158, v38
	v_mov_b32_e32 v159, v39
	v_mov_b32_e32 v160, v16
	v_mov_b32_e32 v161, v17
	v_mov_b32_e32 v162, v18
	v_mov_b32_e32 v163, v19
	v_mov_b32_e32 v164, v20
	v_mov_b32_e32 v165, v21
	v_mov_b32_e32 v166, v22
	v_mov_b32_e32 v167, v23
	v_mov_b32_e32 v168, v24
	v_mov_b32_e32 v169, v25
	v_mov_b32_e32 v170, v26
	v_mov_b32_e32 v171, v27
	v_mov_b32_e32 v172, v28
	v_mov_b32_e32 v173, v29
	v_mov_b32_e32 v174, v30
	v_mov_b32_e32 v175, v31
	v_mov_b32_e32 v176, v32
	v_mov_b32_e32 v177, v33
	v_mov_b32_e32 v178, v34
	v_mov_b32_e32 v179, v35
	v_mov_b32_e32 v180, v36
	v_mov_b32_e32 v181, v37
	v_mov_b32_e32 v182, v38
	v_mov_b32_e32 v183, v39
	v_mov_b32_e32 v184, v16
	v_mov_b32_e32 v185, v17
	v_mov_b32_e32 v186, v18
	v_mov_b32_e32 v187, v19
	v_mov_b32_e32 v188, v20
	v_mov_b32_e32 v189, v21
	v_mov_b32_e32 v190, v22
	v_mov_b32_e32 v191, v23
	v_mov_b32_e32 v192, v24
	v_mov_b32_e32 v193, v25
	v_mov_b32_e32 v194, v26
	v_mov_b32_e32 v195, v27
	v_mov_b32_e32 v196, v28
	v_mov_b32_e32 v197, v29
	v_mov_b32_e32 v198, v30
	v_mov_b32_e32 v199, v31
	v_mov_b32_e32 v200, v32
	v_mov_b32_e32 v201, v33
	v_mov_b32_e32 v202, v34
	v_mov_b32_e32 v203, v35
	v_mov_b32_e32 v204, v36
	v_mov_b32_e32 v205, v37
	v_mov_b32_e32 v206, v38
	v_mov_b32_e32 v207, v39
	v_mov_b32_e32 v208, v16
	v_mov_b32_e32 v209, v17
	v_mov_b32_e32 v210, v18
	v_mov_b32_e32 v211, v19
	v_mov_b32_e32 v212, v20
	v_mov_b32_e32 v213, v21
	v_mov_b32_e32 v214, v22
	v_mov_b32_e32 v215, v23
	v_mov_b32_e32 v216, v24
	v_mov_b32_e32 v217, v25
	v_mov_b32_e32 v218, v26
	v_mov_b32_e32 v219, v27
	v_mov_b32_e32 v220, v28
	v_mov_b32_e32 v221, v29
	v_mov_b32_e32 v222, v30
	v_mov_b32_e32 v223, v31
	v_mov_b32_e32 v224, v32
	v_mov_b32_e32 v225, v33
	v_mov_b32_e32 v226, v34
	v_mov_b32_e32 v227, v35
	v_mov_b32_e32 v228, v36
	v_mov_b32_e32 v229, v37
	v_mov_b32_e32 v230, v38
	v_mov_b32_e32 v231, v39
	v_mov_b32_e32 v232, v16
	v_mov_b32_e32 v233, v17
	v_mov_b32_e32 v234, v18
	v_mov_b32_e32 v235, v19
	v_mov_b32_e32 v236, v20
	v_mov_b32_e32 v237, v21
	v_mov_b32_e32 v238, v22
	v_mov_b32_e32 v239, v23
	v_mov_b32_e32 v240, v24
	v_mov_b32_e32 v241, v25
	v_mov_b32_e32 v242, v26
	v_mov_b32_e32 v243, v27
	v_mov_b32_e32 v244, v28
	v_mov_b32_e32 v245, v29
	v_mov_b32_e32 v246, v30
	v_mov_b32_e32 v247, v31
	v_mov_b32_e32 v248, v32
	v_mov_b32_e32 v249, v33
	v_mov_b32_e32 v250, v34
	v_mov_b32_e32 v251, v35
	v_mov_b32_e32 v252, v36
	v_mov_b32_e32 v253, v37
	v_mov_b32_e32 v254, v38
	v_mov_b32_e32 v255, v39
	s_waitcnt vmcnt(15)
	s_barrier

.Lfc_ng_1:
	s_waitcnt lgkmcnt(0)
	v_mfma_f32_16x16x32_f16 v[64:67], v[16:19], v[40:43], v[64:67]
	v_mfma_f32_16x16x32_f16 v[68:71], v[20:23], v[40:43], v[68:71]
	v_mfma_f32_16x16x32_f16 v[72:75], v[24:27], v[40:43], v[72:75]
	v_mfma_f32_16x16x32_f16 v[76:79], v[28:31], v[40:43], v[76:79]
	v_mfma_f32_16x16x32_f16 v[80:83], v[32:35], v[40:43], v[80:83]
	v_mfma_f32_16x16x32_f16 v[84:87], v[36:39], v[40:43], v[84:87]
	v_mfma_f32_16x16x32_f16 v[88:91], v[16:19], v[44:47], v[88:91]
	ds_read_b128 v[40:43], v1 offset:4096
	v_mfma_f32_16x16x32_f16 v[92:95], v[20:23], v[44:47], v[92:95]
	v_mfma_f32_16x16x32_f16 v[96:99], v[24:27], v[44:47], v[96:99]
	v_mfma_f32_16x16x32_f16 v[100:103], v[28:31], v[44:47], v[100:103]
	v_mfma_f32_16x16x32_f16 v[104:107], v[32:35], v[44:47], v[104:107]
	v_mfma_f32_16x16x32_f16 v[108:111], v[36:39], v[44:47], v[108:111]
	v_mfma_f32_16x16x32_f16 v[112:115], v[16:19], v[48:51], v[112:115]
	ds_read_b128 v[44:47], v1 offset:5120
	v_mfma_f32_16x16x32_f16 v[116:119], v[20:23], v[48:51], v[116:119]
	v_mfma_f32_16x16x32_f16 v[120:123], v[24:27], v[48:51], v[120:123]
	v_mfma_f32_16x16x32_f16 v[124:127], v[28:31], v[48:51], v[124:127]
	v_mfma_f32_16x16x32_f16 v[128:131], v[32:35], v[48:51], v[128:131]
	v_mfma_f32_16x16x32_f16 v[132:135], v[36:39], v[48:51], v[132:135]
	v_mfma_f32_16x16x32_f16 v[136:139], v[16:19], v[52:55], v[136:139]
	ds_read_b128 v[48:51], v1 offset:6144
	v_mfma_f32_16x16x32_f16 v[140:143], v[20:23], v[52:55], v[140:143]
	v_mfma_f32_16x16x32_f16 v[144:147], v[24:27], v[52:55], v[144:147]
	v_mfma_f32_16x16x32_f16 v[148:151], v[28:31], v[52:55], v[148:151]
	v_mfma_f32_16x16x32_f16 v[152:155], v[32:35], v[52:55], v[152:155]
	v_mfma_f32_16x16x32_f16 v[156:159], v[36:39], v[52:55], v[156:159]
	s_waitcnt lgkmcnt(2)
	v_mfma_f32_16x16x32_f16 v[160:163], v[16:19], v[40:43], v[160:163]
	ds_read_b128 v[52:55], v1 offset:7168
	v_mfma_f32_16x16x32_f16 v[164:167], v[20:23], v[40:43], v[164:167]
	v_mfma_f32_16x16x32_f16 v[168:171], v[24:27], v[40:43], v[168:171]
	v_mfma_f32_16x16x32_f16 v[172:175], v[28:31], v[40:43], v[172:175]
	v_mfma_f32_16x16x32_f16 v[176:179], v[32:35], v[40:43], v[176:179]
	v_mfma_f32_16x16x32_f16 v[180:183], v[36:39], v[40:43], v[180:183]
	s_waitcnt lgkmcnt(2)
	v_mfma_f32_16x16x32_f16 v[184:187], v[16:19], v[44:47], v[184:187]
	v_mfma_f32_16x16x32_f16 v[188:191], v[20:23], v[44:47], v[188:191]
	v_mfma_f32_16x16x32_f16 v[192:195], v[24:27], v[44:47], v[192:195]
	v_mfma_f32_16x16x32_f16 v[196:199], v[28:31], v[44:47], v[196:199]
	v_mfma_f32_16x16x32_f16 v[200:203], v[32:35], v[44:47], v[200:203]
	v_mfma_f32_16x16x32_f16 v[204:207], v[36:39], v[44:47], v[204:207]
	s_cmp_eq_u32 s21, 11
	s_cbranch_scc1 .Lfc_w0_2
	s_waitcnt vmcnt(5)
	s_branch .Lfc_w1_2

.Lfc_swd_4:
.Lfc_ng_3:
	s_waitcnt lgkmcnt(0)
	v_mfma_f32_16x16x32_f16 v[64:67], v[16:19], v[40:43], v[64:67]
	v_mfma_f32_16x16x32_f16 v[68:71], v[20:23], v[40:43], v[68:71]
	v_mfma_f32_16x16x32_f16 v[72:75], v[24:27], v[40:43], v[72:75]
	v_mfma_f32_16x16x32_f16 v[76:79], v[28:31], v[40:43], v[76:79]
	v_mfma_f32_16x16x32_f16 v[80:83], v[32:35], v[40:43], v[80:83]
	v_mfma_f32_16x16x32_f16 v[84:87], v[36:39], v[40:43], v[84:87]
	v_mfma_f32_16x16x32_f16 v[88:91], v[16:19], v[44:47], v[88:91]
	ds_read_b128 v[40:43], v1 offset:45056
	v_mfma_f32_16x16x32_f16 v[92:95], v[20:23], v[44:47], v[92:95]
	v_mfma_f32_16x16x32_f16 v[96:99], v[24:27], v[44:47], v[96:99]
	v_mfma_f32_16x16x32_f16 v[100:103], v[28:31], v[44:47], v[100:103]
	v_mfma_f32_16x16x32_f16 v[104:107], v[32:35], v[44:47], v[104:107]
	v_mfma_f32_16x16x32_f16 v[108:111], v[36:39], v[44:47], v[108:111]
	v_mfma_f32_16x16x32_f16 v[112:115], v[16:19], v[48:51], v[112:115]
	ds_read_b128 v[44:47], v1 offset:46080
	v_mfma_f32_16x16x32_f16 v[116:119], v[20:23], v[48:51], v[116:119]
	v_mfma_f32_16x16x32_f16 v[120:123], v[24:27], v[48:51], v[120:123]
	v_mfma_f32_16x16x32_f16 v[124:127], v[28:31], v[48:51], v[124:127]
	v_mfma_f32_16x16x32_f16 v[128:131], v[32:35], v[48:51], v[128:131]
	v_mfma_f32_16x16x32_f16 v[132:135], v[36:39], v[48:51], v[132:135]
	v_mfma_f32_16x16x32_f16 v[136:139], v[16:19], v[52:55], v[136:139]
	ds_read_b128 v[48:51], v1 offset:47104
	v_mfma_f32_16x16x32_f16 v[140:143], v[20:23], v[52:55], v[140:143]
	v_mfma_f32_16x16x32_f16 v[144:147], v[24:27], v[52:55], v[144:147]
	v_mfma_f32_16x16x32_f16 v[148:151], v[28:31], v[52:55], v[148:151]
	v_mfma_f32_16x16x32_f16 v[152:155], v[32:35], v[52:55], v[152:155]
	v_mfma_f32_16x16x32_f16 v[156:159], v[36:39], v[52:55], v[156:159]
	s_waitcnt lgkmcnt(2)
	v_mfma_f32_16x16x32_f16 v[160:163], v[16:19], v[40:43], v[160:163]
	ds_read_b128 v[52:55], v1 offset:48128
	v_mfma_f32_16x16x32_f16 v[164:167], v[20:23], v[40:43], v[164:167]
	v_mfma_f32_16x16x32_f16 v[168:171], v[24:27], v[40:43], v[168:171]
	v_mfma_f32_16x16x32_f16 v[172:175], v[28:31], v[40:43], v[172:175]
	v_mfma_f32_16x16x32_f16 v[176:179], v[32:35], v[40:43], v[176:179]
	v_mfma_f32_16x16x32_f16 v[180:183], v[36:39], v[40:43], v[180:183]
	s_waitcnt lgkmcnt(2)
	v_mfma_f32_16x16x32_f16 v[184:187], v[16:19], v[44:47], v[184:187]
	v_mfma_f32_16x16x32_f16 v[188:191], v[20:23], v[44:47], v[188:191]
	v_mfma_f32_16x16x32_f16 v[192:195], v[24:27], v[44:47], v[192:195]
	v_mfma_f32_16x16x32_f16 v[196:199], v[28:31], v[44:47], v[196:199]
	v_mfma_f32_16x16x32_f16 v[200:203], v[32:35], v[44:47], v[200:203]
	v_mfma_f32_16x16x32_f16 v[204:207], v[36:39], v[44:47], v[204:207]
	s_cmp_eq_u32 s21, 11
	s_cbranch_scc1 .Lfc_w0_5
	s_waitcnt vmcnt(5)
	s_branch .Lfc_w1_5

.Lfc_ng_6:
	s_waitcnt lgkmcnt(0)
	v_mfma_f32_16x16x32_f16 v[64:67], v[16:19], v[40:43], v[64:67]
	v_mfma_f32_16x16x32_f16 v[68:71], v[20:23], v[40:43], v[68:71]
	v_mfma_f32_16x16x32_f16 v[72:75], v[24:27], v[40:43], v[72:75]
	v_mfma_f32_16x16x32_f16 v[76:79], v[28:31], v[40:43], v[76:79]
	v_mfma_f32_16x16x32_f16 v[80:83], v[32:35], v[40:43], v[80:83]
	v_mfma_f32_16x16x32_f16 v[84:87], v[36:39], v[40:43], v[84:87]
	v_mfma_f32_16x16x32_f16 v[88:91], v[16:19], v[44:47], v[88:91]
	ds_read_b128 v[40:43], v2 offset:4096
	v_mfma_f32_16x16x32_f16 v[92:95], v[20:23], v[44:47], v[92:95]
	v_mfma_f32_16x16x32_f16 v[96:99], v[24:27], v[44:47], v[96:99]
	v_mfma_f32_16x16x32_f16 v[100:103], v[28:31], v[44:47], v[100:103]
	v_mfma_f32_16x16x32_f16 v[104:107], v[32:35], v[44:47], v[104:107]
	v_mfma_f32_16x16x32_f16 v[108:111], v[36:39], v[44:47], v[108:111]
	v_mfma_f32_16x16x32_f16 v[112:115], v[16:19], v[48:51], v[112:115]
	ds_read_b128 v[44:47], v2 offset:5120
	v_mfma_f32_16x16x32_f16 v[116:119], v[20:23], v[48:51], v[116:119]
	v_mfma_f32_16x16x32_f16 v[120:123], v[24:27], v[48:51], v[120:123]
	v_mfma_f32_16x16x32_f16 v[124:127], v[28:31], v[48:51], v[124:127]
	v_mfma_f32_16x16x32_f16 v[128:131], v[32:35], v[48:51], v[128:131]
	v_mfma_f32_16x16x32_f16 v[132:135], v[36:39], v[48:51], v[132:135]
	v_mfma_f32_16x16x32_f16 v[136:139], v[16:19], v[52:55], v[136:139]
	ds_read_b128 v[48:51], v2 offset:6144
	v_mfma_f32_16x16x32_f16 v[140:143], v[20:23], v[52:55], v[140:143]
	v_mfma_f32_16x16x32_f16 v[144:147], v[24:27], v[52:55], v[144:147]
	v_mfma_f32_16x16x32_f16 v[148:151], v[28:31], v[52:55], v[148:151]
	v_mfma_f32_16x16x32_f16 v[152:155], v[32:35], v[52:55], v[152:155]
	v_mfma_f32_16x16x32_f16 v[156:159], v[36:39], v[52:55], v[156:159]
	s_waitcnt lgkmcnt(2)
	v_mfma_f32_16x16x32_f16 v[160:163], v[16:19], v[40:43], v[160:163]
	ds_read_b128 v[52:55], v2 offset:7168
	v_mfma_f32_16x16x32_f16 v[164:167], v[20:23], v[40:43], v[164:167]
	v_mfma_f32_16x16x32_f16 v[168:171], v[24:27], v[40:43], v[168:171]
	v_mfma_f32_16x16x32_f16 v[172:175], v[28:31], v[40:43], v[172:175]
	v_mfma_f32_16x16x32_f16 v[176:179], v[32:35], v[40:43], v[176:179]
	v_mfma_f32_16x16x32_f16 v[180:183], v[36:39], v[40:43], v[180:183]
	s_waitcnt lgkmcnt(2)
	v_mfma_f32_16x16x32_f16 v[184:187], v[16:19], v[44:47], v[184:187]
	v_mfma_f32_16x16x32_f16 v[188:191], v[20:23], v[44:47], v[188:191]
	v_mfma_f32_16x16x32_f16 v[192:195], v[24:27], v[44:47], v[192:195]
	v_mfma_f32_16x16x32_f16 v[196:199], v[28:31], v[44:47], v[196:199]
	v_mfma_f32_16x16x32_f16 v[200:203], v[32:35], v[44:47], v[200:203]
	v_mfma_f32_16x16x32_f16 v[204:207], v[36:39], v[44:47], v[204:207]
	s_cmp_eq_u32 s21, 11
	s_cbranch_scc1 .Lfc_w0_7
	s_waitcnt vmcnt(5)
	s_branch .Lfc_w1_7

.Lfc_ng_8:
	s_waitcnt lgkmcnt(0)
	v_mfma_f32_16x16x32_f16 v[64:67], v[16:19], v[40:43], v[64:67]
	v_mfma_f32_16x16x32_f16 v[68:71], v[20:23], v[40:43], v[68:71]
	v_mfma_f32_16x16x32_f16 v[72:75], v[24:27], v[40:43], v[72:75]
	v_mfma_f32_16x16x32_f16 v[76:79], v[28:31], v[40:43], v[76:79]
	v_mfma_f32_16x16x32_f16 v[80:83], v[32:35], v[40:43], v[80:83]
	v_mfma_f32_16x16x32_f16 v[84:87], v[36:39], v[40:43], v[84:87]
	v_mfma_f32_16x16x32_f16 v[88:91], v[16:19], v[44:47], v[88:91]
	ds_read_b128 v[40:43], v2 offset:45056
	v_mfma_f32_16x16x32_f16 v[92:95], v[20:23], v[44:47], v[92:95]
	v_mfma_f32_16x16x32_f16 v[96:99], v[24:27], v[44:47], v[96:99]
	v_mfma_f32_16x16x32_f16 v[100:103], v[28:31], v[44:47], v[100:103]
	v_mfma_f32_16x16x32_f16 v[104:107], v[32:35], v[44:47], v[104:107]
	v_mfma_f32_16x16x32_f16 v[108:111], v[36:39], v[44:47], v[108:111]
	v_mfma_f32_16x16x32_f16 v[112:115], v[16:19], v[48:51], v[112:115]
	ds_read_b128 v[44:47], v2 offset:46080
	v_mfma_f32_16x16x32_f16 v[116:119], v[20:23], v[48:51], v[116:119]
	v_mfma_f32_16x16x32_f16 v[120:123], v[24:27], v[48:51], v[120:123]
	v_mfma_f32_16x16x32_f16 v[124:127], v[28:31], v[48:51], v[124:127]
	v_mfma_f32_16x16x32_f16 v[128:131], v[32:35], v[48:51], v[128:131]
	v_mfma_f32_16x16x32_f16 v[132:135], v[36:39], v[48:51], v[132:135]
	v_mfma_f32_16x16x32_f16 v[136:139], v[16:19], v[52:55], v[136:139]
	ds_read_b128 v[48:51], v2 offset:47104
	v_mfma_f32_16x16x32_f16 v[140:143], v[20:23], v[52:55], v[140:143]
	v_mfma_f32_16x16x32_f16 v[144:147], v[24:27], v[52:55], v[144:147]
	v_mfma_f32_16x16x32_f16 v[148:151], v[28:31], v[52:55], v[148:151]
	v_mfma_f32_16x16x32_f16 v[152:155], v[32:35], v[52:55], v[152:155]
	v_mfma_f32_16x16x32_f16 v[156:159], v[36:39], v[52:55], v[156:159]
	s_waitcnt lgkmcnt(2)
	v_mfma_f32_16x16x32_f16 v[160:163], v[16:19], v[40:43], v[160:163]
	ds_read_b128 v[52:55], v2 offset:48128
	v_mfma_f32_16x16x32_f16 v[164:167], v[20:23], v[40:43], v[164:167]
	v_mfma_f32_16x16x32_f16 v[168:171], v[24:27], v[40:43], v[168:171]
	v_mfma_f32_16x16x32_f16 v[172:175], v[28:31], v[40:43], v[172:175]
	v_mfma_f32_16x16x32_f16 v[176:179], v[32:35], v[40:43], v[176:179]
	v_mfma_f32_16x16x32_f16 v[180:183], v[36:39], v[40:43], v[180:183]
	s_waitcnt lgkmcnt(2)
	v_mfma_f32_16x16x32_f16 v[184:187], v[16:19], v[44:47], v[184:187]
	v_mfma_f32_16x16x32_f16 v[188:191], v[20:23], v[44:47], v[188:191]
	v_mfma_f32_16x16x32_f16 v[192:195], v[24:27], v[44:47], v[192:195]
	v_mfma_f32_16x16x32_f16 v[196:199], v[28:31], v[44:47], v[196:199]
	v_mfma_f32_16x16x32_f16 v[200:203], v[32:35], v[44:47], v[200:203]
	v_mfma_f32_16x16x32_f16 v[204:207], v[36:39], v[44:47], v[204:207]
	s_cmp_eq_u32 s21, 11
	s_cbranch_scc1 .Lfc_w0_9
	s_waitcnt vmcnt(5)
	s_branch .Lfc_w1_9

.Lfc_h1_entry:
	s_setprio 1
	s_add_u32 m0, s22, 0x0
	s_nop 0
	global_load_lds_dwordx4 v5, s[24:25]
	s_add_u32 m0, s22, 0x400
	s_nop 0
	global_load_lds_dwordx4 v6, s[24:25]
	s_add_u32 m0, s23, 0x0
	s_nop 0
	global_load_lds_dwordx4 v11, s[28:29]
	s_add_u32 m0, s23, 0x400
	s_nop 0
	global_load_lds_dwordx4 v11, s[32:33]
	s_add_u32 m0, s23, 0x800
	s_nop 0
	global_load_lds_dwordx4 v11, s[36:37]
	s_add_u32 s24, s24, 0x80
	s_addc_u32 s25, s25, 0
	s_add_u32 s28, s28, 0x30000
	s_addc_u32 s29, s29, 0
	s_add_u32 s32, s32, 0x30000
	s_addc_u32 s33, s33, 0
	s_add_u32 s36, s36, 0x30000
	s_addc_u32 s37, s37, 0
	s_add_u32 m0, s22, 0xa000
	s_nop 0
	global_load_lds_dwordx4 v5, s[26:27]
	s_add_u32 m0, s22, 0xa400
	s_nop 0
	global_load_lds_dwordx4 v6, s[26:27]
	s_add_u32 m0, s23, 0xa000
	s_nop 0
	global_load_lds_dwordx4 v11, s[30:31]
	s_add_u32 m0, s23, 0xa400
	s_nop 0
	global_load_lds_dwordx4 v11, s[34:35]
	s_add_u32 m0, s23, 0xa800
	s_nop 0
	global_load_lds_dwordx4 v11, s[38:39]
	s_add_u32 s26, s26, 0x80
	s_addc_u32 s27, s27, 0
	s_add_u32 s30, s30, 0x30000
	s_addc_u32 s31, s31, 0
	s_add_u32 s34, s34, 0x30000
	s_addc_u32 s35, s35, 0
	s_add_u32 s38, s38, 0x30000
	s_addc_u32 s39, s39, 0
	s_add_u32 m0, s22, 0x14000
	s_nop 0
	global_load_lds_dwordx4 v5, s[24:25]
	s_add_u32 m0, s22, 0x14400
	s_nop 0
	global_load_lds_dwordx4 v6, s[24:25]
	s_add_u32 m0, s23, 0x14000
	s_nop 0
	global_load_lds_dwordx4 v11, s[28:29]
	s_add_u32 m0, s23, 0x14400
	s_nop 0
	global_load_lds_dwordx4 v11, s[32:33]
	s_add_u32 m0, s23, 0x14800
	s_nop 0
	global_load_lds_dwordx4 v11, s[36:37]
	s_add_u32 s24, s24, 0x80
	s_addc_u32 s25, s25, 0
	s_add_u32 s28, s28, 0x30000
	s_addc_u32 s29, s29, 0
	s_add_u32 s32, s32, 0x30000
	s_addc_u32 s33, s33, 0
	s_add_u32 s36, s36, 0x30000
	s_addc_u32 s37, s37, 0
	s_add_u32 m0, s22, 0x1e000
	s_nop 0
	global_load_lds_dwordx4 v5, s[26:27]
	s_add_u32 m0, s22, 0x1e400
	s_nop 0
	global_load_lds_dwordx4 v6, s[26:27]
	s_add_u32 m0, s23, 0x1e000
	s_nop 0
	global_load_lds_dwordx4 v11, s[30:31]
	s_add_u32 m0, s23, 0x1e400
	s_nop 0
	global_load_lds_dwordx4 v11, s[34:35]
	s_add_u32 m0, s23, 0x1e800
	s_nop 0
	global_load_lds_dwordx4 v11, s[38:39]
	s_add_u32 s26, s26, 0x80
	s_addc_u32 s27, s27, 0
	s_add_u32 s30, s30, 0x30000
	s_addc_u32 s31, s31, 0
	s_add_u32 s34, s34, 0x30000
	s_addc_u32 s35, s35, 0
	s_add_u32 s38, s38, 0x30000
	s_addc_u32 s39, s39, 0
	s_waitcnt vmcnt(20)
	v_med3_i32 v64, v64, 0, s93
	v_med3_i32 v65, v65, 1, s94
	v_med3_i32 v66, v66, 0, s93
	v_med3_i32 v67, v67, 1, s94
	v_add_u32_e32 v64, s92, v64
	v_add_u32_e32 v66, s92, v66
	v_add_u32_e32 v65, s92, v65
	v_add_u32_e32 v67, s92, v67
	v_add_u32_e32 v65, -1, v65
	v_add_u32_e32 v67, -1, v67
	v_lshl_add_u32 v7, v64, 10, v71
	v_lshl_add_u32 v8, v66, 10, v71
	v_lshl_add_u32 v9, v65, 10, v71
	v_lshl_add_u32 v10, v67, 10, v71
	v_cvt_pk_f16_f32 v12, v40, v41
	v_cvt_pk_f16_f32 v13, v42, v43
	v_cvt_pk_f16_f32 v14, v44, v45
	v_cvt_pk_f16_f32 v15, v46, v47
	v_cvt_pk_f16_f32 v56, v56, v57
	v_cvt_pk_f16_f32 v57, v58, v59
	v_cvt_pk_f16_f32 v58, v60, v61
	v_cvt_pk_f16_f32 v59, v62, v63
	v_cvt_pk_f16_f32 v60, v48, v49
	v_cvt_pk_f16_f32 v61, v50, v51
	v_cvt_pk_f16_f32 v62, v52, v53
	v_cvt_pk_f16_f32 v63, v54, v55
	v_mov_b32_e32 v64, v16
	v_mov_b32_e32 v65, v17
	v_mov_b32_e32 v66, v18
	v_mov_b32_e32 v67, v19
	v_mov_b32_e32 v68, v20
	v_mov_b32_e32 v69, v21
	v_mov_b32_e32 v70, v22
	v_mov_b32_e32 v71, v23
	v_mov_b32_e32 v72, v24
	v_mov_b32_e32 v73, v25
	v_mov_b32_e32 v74, v26
	v_mov_b32_e32 v75, v27
	v_mov_b32_e32 v76, v28
	v_mov_b32_e32 v77, v29
	v_mov_b32_e32 v78, v30
	v_mov_b32_e32 v79, v31
	v_mov_b32_e32 v80, v32
	v_mov_b32_e32 v81, v33
	v_mov_b32_e32 v82, v34
	v_mov_b32_e32 v83, v35
	v_mov_b32_e32 v84, v36
	v_mov_b32_e32 v85, v37
	v_mov_b32_e32 v86, v38
	v_mov_b32_e32 v87, v39
	v_mov_b32_e32 v88, v16
	v_mov_b32_e32 v89, v17
	v_mov_b32_e32 v90, v18
	v_mov_b32_e32 v91, v19
	v_mov_b32_e32 v92, v20
	v_mov_b32_e32 v93, v21
	v_mov_b32_e32 v94, v22
	v_mov_b32_e32 v95, v23
	v_mov_b32_e32 v96, v24
	v_mov_b32_e32 v97, v25
	v_mov_b32_e32 v98, v26
	v_mov_b32_e32 v99, v27
	v_mov_b32_e32 v100, v28
	v_mov_b32_e32 v101, v29
	v_mov_b32_e32 v102, v30
	v_mov_b32_e32 v103, v31
	v_mov_b32_e32 v104, v32
	v_mov_b32_e32 v105, v33
	v_mov_b32_e32 v106, v34
	v_mov_b32_e32 v107, v35
	v_mov_b32_e32 v108, v36
	v_mov_b32_e32 v109, v37
	v_mov_b32_e32 v110, v38
	v_mov_b32_e32 v111, v39
	v_mov_b32_e32 v112, v16
	v_mov_b32_e32 v113, v17
	v_mov_b32_e32 v114, v18
	v_mov_b32_e32 v115, v19
	v_mov_b32_e32 v116, v20
	v_mov_b32_e32 v117, v21
	v_mov_b32_e32 v118, v22
	v_mov_b32_e32 v119, v23
	v_mov_b32_e32 v120, v24
	v_mov_b32_e32 v121, v25
	v_mov_b32_e32 v122, v26
	v_mov_b32_e32 v123, v27
	v_mov_b32_e32 v124, v28
	v_mov_b32_e32 v125, v29
	v_mov_b32_e32 v126, v30
	v_mov_b32_e32 v127, v31
	v_mov_b32_e32 v128, v32
	v_mov_b32_e32 v129, v33
	v_mov_b32_e32 v130, v34
	v_mov_b32_e32 v131, v35
	v_mov_b32_e32 v132, v36
	v_mov_b32_e32 v133, v37
	v_mov_b32_e32 v134, v38
	v_mov_b32_e32 v135, v39
	v_mov_b32_e32 v136, v16
	v_mov_b32_e32 v137, v17
	v_mov_b32_e32 v138, v18
	v_mov_b32_e32 v139, v19
	v_mov_b32_e32 v140, v20
	v_mov_b32_e32 v141, v21
	v_mov_b32_e32 v142, v22
	v_mov_b32_e32 v143, v23
	v_mov_b32_e32 v144, v24
	v_mov_b32_e32 v145, v25
	v_mov_b32_e32 v146, v26
	v_mov_b32_e32 v147, v27
	v_mov_b32_e32 v148, v28
	v_mov_b32_e32 v149, v29
	v_mov_b32_e32 v150, v30
	v_mov_b32_e32 v151, v31
	v_mov_b32_e32 v152, v32
	v_mov_b32_e32 v153, v33
	v_mov_b32_e32 v154, v34
	v_mov_b32_e32 v155, v35
	v_mov_b32_e32 v156, v36
	v_mov_b32_e32 v157, v37
	v_mov_b32_e32 v158, v38
	v_mov_b32_e32 v159, v39
	v_mov_b32_e32 v160, v16
	v_mov_b32_e32 v161, v17
	v_mov_b32_e32 v162, v18
	v_mov_b32_e32 v163, v19
	v_mov_b32_e32 v164, v20
	v_mov_b32_e32 v165, v21
	v_mov_b32_e32 v166, v22
	v_mov_b32_e32 v167, v23
	v_mov_b32_e32 v168, v24
	v_mov_b32_e32 v169, v25
	v_mov_b32_e32 v170, v26
	v_mov_b32_e32 v171, v27
	v_mov_b32_e32 v172, v28
	v_mov_b32_e32 v173, v29
	v_mov_b32_e32 v174, v30
	v_mov_b32_e32 v175, v31
	v_mov_b32_e32 v176, v32
	v_mov_b32_e32 v177, v33
	v_mov_b32_e32 v178, v34
	v_mov_b32_e32 v179, v35
	v_mov_b32_e32 v180, v36
	v_mov_b32_e32 v181, v37
	v_mov_b32_e32 v182, v38
	v_mov_b32_e32 v183, v39
	v_mov_b32_e32 v184, v16
	v_mov_b32_e32 v185, v17
	v_mov_b32_e32 v186, v18
	v_mov_b32_e32 v187, v19
	v_mov_b32_e32 v188, v20
	v_mov_b32_e32 v189, v21
	v_mov_b32_e32 v190, v22
	v_mov_b32_e32 v191, v23
	v_mov_b32_e32 v192, v24
	v_mov_b32_e32 v193, v25
	v_mov_b32_e32 v194, v26
	v_mov_b32_e32 v195, v27
	v_mov_b32_e32 v196, v28
	v_mov_b32_e32 v197, v29
	v_mov_b32_e32 v198, v30
	v_mov_b32_e32 v199, v31
	v_mov_b32_e32 v200, v32
	v_mov_b32_e32 v201, v33
	v_mov_b32_e32 v202, v34
	v_mov_b32_e32 v203, v35
	v_mov_b32_e32 v204, v36
	v_mov_b32_e32 v205, v37
	v_mov_b32_e32 v206, v38
	v_mov_b32_e32 v207, v39
	v_mov_b32_e32 v208, v16
	v_mov_b32_e32 v209, v17
	v_mov_b32_e32 v210, v18
	v_mov_b32_e32 v211, v19
	v_mov_b32_e32 v212, v20
	v_mov_b32_e32 v213, v21
	v_mov_b32_e32 v214, v22
	v_mov_b32_e32 v215, v23
	v_mov_b32_e32 v216, v24
	v_mov_b32_e32 v217, v25
	v_mov_b32_e32 v218, v26
	v_mov_b32_e32 v219, v27
	v_mov_b32_e32 v220, v28
	v_mov_b32_e32 v221, v29
	v_mov_b32_e32 v222, v30
	v_mov_b32_e32 v223, v31
	v_mov_b32_e32 v224, v32
	v_mov_b32_e32 v225, v33
	v_mov_b32_e32 v226, v34
	v_mov_b32_e32 v227, v35
	v_mov_b32_e32 v228, v36
	v_mov_b32_e32 v229, v37
	v_mov_b32_e32 v230, v38
	v_mov_b32_e32 v231, v39
	v_mov_b32_e32 v232, v16
	v_mov_b32_e32 v233, v17
	v_mov_b32_e32 v234, v18
	v_mov_b32_e32 v235, v19
	v_mov_b32_e32 v236, v20
	v_mov_b32_e32 v237, v21
	v_mov_b32_e32 v238, v22
	v_mov_b32_e32 v239, v23
	v_mov_b32_e32 v240, v24
	v_mov_b32_e32 v241, v25
	v_mov_b32_e32 v242, v26
	v_mov_b32_e32 v243, v27
	v_mov_b32_e32 v244, v28
	v_mov_b32_e32 v245, v29
	v_mov_b32_e32 v246, v30
	v_mov_b32_e32 v247, v31
	v_mov_b32_e32 v248, v32
	v_mov_b32_e32 v249, v33
	v_mov_b32_e32 v250, v34
	v_mov_b32_e32 v251, v35
	v_mov_b32_e32 v252, v36
	v_mov_b32_e32 v253, v37
	v_mov_b32_e32 v254, v38
	v_mov_b32_e32 v255, v39
	s_waitcnt vmcnt(15)
	s_barrier
	ds_read_b128 v[16:19], v3 offset:0
	ds_read_b128 v[20:23], v3 offset:1024
	ds_read_b128 v[24:27], v3 offset:2048
	ds_read_b128 v[28:31], v3 offset:3072
	ds_read_b128 v[32:35], v3 offset:4096
	ds_read_b128 v[36:39], v3 offset:5120
	ds_read_b128 v[40:43], v1 offset:0
	ds_read_b128 v[44:47], v1 offset:1024
	ds_read_b128 v[48:51], v1 offset:2048
	ds_read_b128 v[52:55], v1 offset:3072
	s_waitcnt vmcnt(10)
	s_barrier
.Lfc_h1_loop:
	s_waitcnt lgkmcnt(0)
	v_mfma_f32_16x16x32_f16 v[64:67], v[16:19], v[40:43], v[64:67]
	v_mfma_f32_16x16x32_f16 v[68:71], v[20:23], v[40:43], v[68:71]
	v_mfma_f32_16x16x32_f16 v[72:75], v[24:27], v[40:43], v[72:75]
	v_mfma_f32_16x16x32_f16 v[76:79], v[28:31], v[40:43], v[76:79]
	v_mfma_f32_16x16x32_f16 v[80:83], v[32:35], v[40:43], v[80:83]
	v_mfma_f32_16x16x32_f16 v[84:87], v[36:39], v[40:43], v[84:87]
	v_mfma_f32_16x16x32_f16 v[88:91], v[16:19], v[44:47], v[88:91]
	ds_read_b128 v[40:43], v1 offset:4096
	v_mfma_f32_16x16x32_f16 v[92:95], v[20:23], v[44:47], v[92:95]
	v_mfma_f32_16x16x32_f16 v[96:99], v[24:27], v[44:47], v[96:99]
	v_mfma_f32_16x16x32_f16 v[100:103], v[28:31], v[44:47], v[100:103]
	v_mfma_f32_16x16x32_f16 v[104:107], v[32:35], v[44:47], v[104:107]
	v_mfma_f32_16x16x32_f16 v[108:111], v[36:39], v[44:47], v[108:111]
	v_mfma_f32_16x16x32_f16 v[112:115], v[16:19], v[48:51], v[112:115]
	ds_read_b128 v[44:47], v1 offset:5120
	v_mfma_f32_16x16x32_f16 v[116:119], v[20:23], v[48:51], v[116:119]
	v_mfma_f32_16x16x32_f16 v[120:123], v[24:27], v[48:51], v[120:123]
	v_mfma_f32_16x16x32_f16 v[124:127], v[28:31], v[48:51], v[124:127]
	v_mfma_f32_16x16x32_f16 v[128:131], v[32:35], v[48:51], v[128:131]
	v_mfma_f32_16x16x32_f16 v[132:135], v[36:39], v[48:51], v[132:135]
	v_mfma_f32_16x16x32_f16 v[136:139], v[16:19], v[52:55], v[136:139]
	ds_read_b128 v[48:51], v1 offset:6144
	v_mfma_f32_16x16x32_f16 v[140:143], v[20:23], v[52:55], v[140:143]
	v_mfma_f32_16x16x32_f16 v[144:147], v[24:27], v[52:55], v[144:147]
	v_mfma_f32_16x16x32_f16 v[148:151], v[28:31], v[52:55], v[148:151]
	v_mfma_f32_16x16x32_f16 v[152:155], v[32:35], v[52:55], v[152:155]
	v_mfma_f32_16x16x32_f16 v[156:159], v[36:39], v[52:55], v[156:159]
	s_waitcnt lgkmcnt(2)
	v_mfma_f32_16x16x32_f16 v[160:163], v[16:19], v[40:43], v[160:163]
	ds_read_b128 v[52:55], v1 offset:7168
	v_mfma_f32_16x16x32_f16 v[164:167], v[20:23], v[40:43], v[164:167]
	v_mfma_f32_16x16x32_f16 v[168:171], v[24:27], v[40:43], v[168:171]
	v_mfma_f32_16x16x32_f16 v[172:175], v[28:31], v[40:43], v[172:175]
	v_mfma_f32_16x16x32_f16 v[176:179], v[32:35], v[40:43], v[176:179]
	v_mfma_f32_16x16x32_f16 v[180:183], v[36:39], v[40:43], v[180:183]
	s_waitcnt lgkmcnt(2)
	v_mfma_f32_16x16x32_f16 v[184:187], v[16:19], v[44:47], v[184:187]
	v_mfma_f32_16x16x32_f16 v[188:191], v[20:23], v[44:47], v[188:191]
	v_mfma_f32_16x16x32_f16 v[192:195], v[24:27], v[44:47], v[192:195]
	v_mfma_f32_16x16x32_f16 v[196:199], v[28:31], v[44:47], v[196:199]
	v_mfma_f32_16x16x32_f16 v[200:203], v[32:35], v[44:47], v[200:203]
	v_mfma_f32_16x16x32_f16 v[204:207], v[36:39], v[44:47], v[204:207]
	s_waitcnt lgkmcnt(1)
	v_mfma_f32_16x16x32_f16 v[208:211], v[16:19], v[48:51], v[208:211]
	v_mfma_f32_16x16x32_f16 v[212:215], v[20:23], v[48:51], v[212:215]
	v_mfma_f32_16x16x32_f16 v[216:219], v[24:27], v[48:51], v[216:219]
	v_mfma_f32_16x16x32_f16 v[220:223], v[28:31], v[48:51], v[220:223]
	v_mfma_f32_16x16x32_f16 v[224:227], v[32:35], v[48:51], v[224:227]
	v_mfma_f32_16x16x32_f16 v[228:231], v[36:39], v[48:51], v[228:231]
	s_waitcnt lgkmcnt(0)
	v_mfma_f32_16x16x32_f16 v[232:235], v[16:19], v[52:55], v[232:235]
	v_mfma_f32_16x16x32_f16 v[236:239], v[20:23], v[52:55], v[236:239]
	v_mfma_f32_16x16x32_f16 v[240:243], v[24:27], v[52:55], v[240:243]
	v_mfma_f32_16x16x32_f16 v[244:247], v[28:31], v[52:55], v[244:247]
	v_mfma_f32_16x16x32_f16 v[248:251], v[32:35], v[52:55], v[248:251]
	v_mfma_f32_16x16x32_f16 v[252:255], v[36:39], v[52:55], v[252:255]
	ds_read_b128 v[16:19], v3 offset:40960
	ds_read_b128 v[20:23], v3 offset:41984
	ds_read_b128 v[24:27], v3 offset:43008
	ds_read_b128 v[28:31], v3 offset:44032
	ds_read_b128 v[32:35], v3 offset:45056
	ds_read_b128 v[36:39], v3 offset:46080
	ds_read_b128 v[40:43], v1 offset:40960
	ds_read_b128 v[44:47], v1 offset:41984
	ds_read_b128 v[48:51], v1 offset:43008
	ds_read_b128 v[52:55], v1 offset:44032
	s_cmp_eq_u32 s21, 0
	s_cbranch_scc1 .Lfc_ng_10
	s_add_u32 m0, s22, 0x1e000
	s_nop 0
	global_load_lds_dwordx4 v5, s[26:27]
	s_add_u32 m0, s22, 0x1e400
	s_nop 0
	global_load_lds_dwordx4 v6, s[26:27]
	s_add_u32 m0, s23, 0x1e000
	s_nop 0
	global_load_lds_dwordx4 v11, s[30:31]
	s_add_u32 m0, s23, 0x1e400
	s_nop 0
	global_load_lds_dwordx4 v11, s[34:35]
	s_add_u32 m0, s23, 0x1e800
	s_nop 0
	global_load_lds_dwordx4 v11, s[38:39]
	s_add_u32 s26, s26, 0x80
	s_addc_u32 s27, s27, 0
	s_add_u32 s30, s30, 0x30000
	s_addc_u32 s31, s31, 0
	s_add_u32 s34, s34, 0x30000
	s_addc_u32 s35, s35, 0
	s_add_u32 s38, s38, 0x30000
	s_addc_u32 s39, s39, 0
	s_cmp_eq_u32 s21, 3
	s_cbranch_scc1 .Lfc_sw_11
	s_cmp_eq_u32 s21, 7
	s_cbranch_scc0 .Lfc_swd_11
	s_add_u32 s28, s28, 0x180000
	s_addc_u32 s29, s29, 0
	s_add_u32 s30, s30, 0x180000
	s_addc_u32 s31, s31, 0
	s_add_u32 s32, s32, 0x180000
	s_addc_u32 s33, s33, 0
	s_add_u32 s34, s34, 0x180000
	s_addc_u32 s35, s35, 0
	s_add_u32 s36, s36, 0x180000
	s_addc_u32 s37, s37, 0
	s_add_u32 s38, s38, 0x180000
	s_addc_u32 s39, s39, 0
	s_branch .Lfc_sw2_11

.Lfc_swd_11:
.Lfc_ng_10:
	s_cmp_eq_u32 s21, 11
	s_cbranch_scc1 .Lfc_w0_12
	s_waitcnt vmcnt(5)
	s_branch .Lfc_w1_12

.Lfc_w1_12:
	s_barrier
	s_waitcnt lgkmcnt(0)
	v_mfma_f32_16x16x32_f16 v[64:67], v[16:19], v[40:43], v[64:67]
	v_mfma_f32_16x16x32_f16 v[68:71], v[20:23], v[40:43], v[68:71]
	v_mfma_f32_16x16x32_f16 v[72:75], v[24:27], v[40:43], v[72:75]
	v_mfma_f32_16x16x32_f16 v[76:79], v[28:31], v[40:43], v[76:79]
	v_mfma_f32_16x16x32_f16 v[80:83], v[32:35], v[40:43], v[80:83]
	v_mfma_f32_16x16x32_f16 v[84:87], v[36:39], v[40:43], v[84:87]
	v_mfma_f32_16x16x32_f16 v[88:91], v[16:19], v[44:47], v[88:91]
	ds_read_b128 v[40:43], v1 offset:45056
	v_mfma_f32_16x16x32_f16 v[92:95], v[20:23], v[44:47], v[92:95]
	v_mfma_f32_16x16x32_f16 v[96:99], v[24:27], v[44:47], v[96:99]
	v_mfma_f32_16x16x32_f16 v[100:103], v[28:31], v[44:47], v[100:103]
	v_mfma_f32_16x16x32_f16 v[104:107], v[32:35], v[44:47], v[104:107]
	v_mfma_f32_16x16x32_f16 v[108:111], v[36:39], v[44:47], v[108:111]
	v_mfma_f32_16x16x32_f16 v[112:115], v[16:19], v[48:51], v[112:115]
	ds_read_b128 v[44:47], v1 offset:46080
	v_mfma_f32_16x16x32_f16 v[116:119], v[20:23], v[48:51], v[116:119]
	v_mfma_f32_16x16x32_f16 v[120:123], v[24:27], v[48:51], v[120:123]
	v_mfma_f32_16x16x32_f16 v[124:127], v[28:31], v[48:51], v[124:127]
	v_mfma_f32_16x16x32_f16 v[128:131], v[32:35], v[48:51], v[128:131]
	v_mfma_f32_16x16x32_f16 v[132:135], v[36:39], v[48:51], v[132:135]
	v_mfma_f32_16x16x32_f16 v[136:139], v[16:19], v[52:55], v[136:139]
	ds_read_b128 v[48:51], v1 offset:47104
	v_mfma_f32_16x16x32_f16 v[140:143], v[20:23], v[52:55], v[140:143]
	v_mfma_f32_16x16x32_f16 v[144:147], v[24:27], v[52:55], v[144:147]
	v_mfma_f32_16x16x32_f16 v[148:151], v[28:31], v[52:55], v[148:151]
	v_mfma_f32_16x16x32_f16 v[152:155], v[32:35], v[52:55], v[152:155]
	v_mfma_f32_16x16x32_f16 v[156:159], v[36:39], v[52:55], v[156:159]
	s_waitcnt lgkmcnt(2)
	v_mfma_f32_16x16x32_f16 v[160:163], v[16:19], v[40:43], v[160:163]
	ds_read_b128 v[52:55], v1 offset:48128
	v_mfma_f32_16x16x32_f16 v[164:167], v[20:23], v[40:43], v[164:167]
	v_mfma_f32_16x16x32_f16 v[168:171], v[24:27], v[40:43], v[168:171]
	v_mfma_f32_16x16x32_f16 v[172:175], v[28:31], v[40:43], v[172:175]
	v_mfma_f32_16x16x32_f16 v[176:179], v[32:35], v[40:43], v[176:179]
	v_mfma_f32_16x16x32_f16 v[180:183], v[36:39], v[40:43], v[180:183]
	s_waitcnt lgkmcnt(2)
	v_mfma_f32_16x16x32_f16 v[184:187], v[16:19], v[44:47], v[184:187]
	v_mfma_f32_16x16x32_f16 v[188:191], v[20:23], v[44:47], v[188:191]
	v_mfma_f32_16x16x32_f16 v[192:195], v[24:27], v[44:47], v[192:195]
	v_mfma_f32_16x16x32_f16 v[196:199], v[28:31], v[44:47], v[196:199]
	v_mfma_f32_16x16x32_f16 v[200:203], v[32:35], v[44:47], v[200:203]
	v_mfma_f32_16x16x32_f16 v[204:207], v[36:39], v[44:47], v[204:207]
	s_waitcnt lgkmcnt(1)
	v_mfma_f32_16x16x32_f16 v[208:211], v[16:19], v[48:51], v[208:211]
	v_mfma_f32_16x16x32_f16 v[212:215], v[20:23], v[48:51], v[212:215]
	v_mfma_f32_16x16x32_f16 v[216:219], v[24:27], v[48:51], v[216:219]
	v_mfma_f32_16x16x32_f16 v[220:223], v[28:31], v[48:51], v[220:223]
	v_mfma_f32_16x16x32_f16 v[224:227], v[32:35], v[48:51], v[224:227]
	v_mfma_f32_16x16x32_f16 v[228:231], v[36:39], v[48:51], v[228:231]
	s_waitcnt lgkmcnt(0)
	v_mfma_f32_16x16x32_f16 v[232:235], v[16:19], v[52:55], v[232:235]
	v_mfma_f32_16x16x32_f16 v[236:239], v[20:23], v[52:55], v[236:239]
	v_mfma_f32_16x16x32_f16 v[240:243], v[24:27], v[52:55], v[240:243]
	v_mfma_f32_16x16x32_f16 v[244:247], v[28:31], v[52:55], v[244:247]
	v_mfma_f32_16x16x32_f16 v[248:251], v[32:35], v[52:55], v[248:251]
	v_mfma_f32_16x16x32_f16 v[252:255], v[36:39], v[52:55], v[252:255]
	ds_read_b128 v[16:19], v4 offset:0
	ds_read_b128 v[20:23], v4 offset:1024
	ds_read_b128 v[24:27], v4 offset:2048
	ds_read_b128 v[28:31], v4 offset:3072
	ds_read_b128 v[32:35], v4 offset:4096
	ds_read_b128 v[36:39], v4 offset:5120
	ds_read_b128 v[40:43], v2 offset:0
	ds_read_b128 v[44:47], v2 offset:1024
	ds_read_b128 v[48:51], v2 offset:2048
	ds_read_b128 v[52:55], v2 offset:3072
	s_cmp_eq_u32 s21, 11
	s_cbranch_scc1 .Lfc_ng_13
	s_add_u32 m0, s22, 0x0
	s_nop 0
	global_load_lds_dwordx4 v5, s[24:25]
	s_add_u32 m0, s22, 0x400
	s_nop 0
	global_load_lds_dwordx4 v6, s[24:25]
	s_add_u32 m0, s23, 0x0
	s_nop 0
	global_load_lds_dwordx4 v11, s[28:29]
	s_add_u32 m0, s23, 0x400
	s_nop 0
	global_load_lds_dwordx4 v11, s[32:33]
	s_add_u32 m0, s23, 0x800
	s_nop 0
	global_load_lds_dwordx4 v11, s[36:37]
	s_add_u32 s24, s24, 0x80
	s_addc_u32 s25, s25, 0
	s_add_u32 s28, s28, 0x30000
	s_addc_u32 s29, s29, 0
	s_add_u32 s32, s32, 0x30000
	s_addc_u32 s33, s33, 0
	s_add_u32 s36, s36, 0x30000
	s_addc_u32 s37, s37, 0
.Lfc_ng_13:
	s_cmp_eq_u32 s21, 11
	s_cbranch_scc1 .Lfc_w0_14
	s_waitcnt vmcnt(5)
	s_branch .Lfc_w1_14

.Lfc_w1_14:
	s_barrier
	s_waitcnt lgkmcnt(0)
	v_mfma_f32_16x16x32_f16 v[64:67], v[16:19], v[40:43], v[64:67]
	v_mfma_f32_16x16x32_f16 v[68:71], v[20:23], v[40:43], v[68:71]
	v_mfma_f32_16x16x32_f16 v[72:75], v[24:27], v[40:43], v[72:75]
	v_mfma_f32_16x16x32_f16 v[76:79], v[28:31], v[40:43], v[76:79]
	v_mfma_f32_16x16x32_f16 v[80:83], v[32:35], v[40:43], v[80:83]
	v_mfma_f32_16x16x32_f16 v[84:87], v[36:39], v[40:43], v[84:87]
	v_mfma_f32_16x16x32_f16 v[88:91], v[16:19], v[44:47], v[88:91]
	ds_read_b128 v[40:43], v2 offset:4096
	v_mfma_f32_16x16x32_f16 v[92:95], v[20:23], v[44:47], v[92:95]
	v_mfma_f32_16x16x32_f16 v[96:99], v[24:27], v[44:47], v[96:99]
	v_mfma_f32_16x16x32_f16 v[100:103], v[28:31], v[44:47], v[100:103]
	v_mfma_f32_16x16x32_f16 v[104:107], v[32:35], v[44:47], v[104:107]
	v_mfma_f32_16x16x32_f16 v[108:111], v[36:39], v[44:47], v[108:111]
	v_mfma_f32_16x16x32_f16 v[112:115], v[16:19], v[48:51], v[112:115]
	ds_read_b128 v[44:47], v2 offset:5120
	v_mfma_f32_16x16x32_f16 v[116:119], v[20:23], v[48:51], v[116:119]
	v_mfma_f32_16x16x32_f16 v[120:123], v[24:27], v[48:51], v[120:123]
	v_mfma_f32_16x16x32_f16 v[124:127], v[28:31], v[48:51], v[124:127]
	v_mfma_f32_16x16x32_f16 v[128:131], v[32:35], v[48:51], v[128:131]
	v_mfma_f32_16x16x32_f16 v[132:135], v[36:39], v[48:51], v[132:135]
	v_mfma_f32_16x16x32_f16 v[136:139], v[16:19], v[52:55], v[136:139]
	ds_read_b128 v[48:51], v2 offset:6144
	v_mfma_f32_16x16x32_f16 v[140:143], v[20:23], v[52:55], v[140:143]
	v_mfma_f32_16x16x32_f16 v[144:147], v[24:27], v[52:55], v[144:147]
	v_mfma_f32_16x16x32_f16 v[148:151], v[28:31], v[52:55], v[148:151]
	v_mfma_f32_16x16x32_f16 v[152:155], v[32:35], v[52:55], v[152:155]
	v_mfma_f32_16x16x32_f16 v[156:159], v[36:39], v[52:55], v[156:159]
	s_waitcnt lgkmcnt(2)
	v_mfma_f32_16x16x32_f16 v[160:163], v[16:19], v[40:43], v[160:163]
	ds_read_b128 v[52:55], v2 offset:7168
	v_mfma_f32_16x16x32_f16 v[164:167], v[20:23], v[40:43], v[164:167]
	v_mfma_f32_16x16x32_f16 v[168:171], v[24:27], v[40:43], v[168:171]
	v_mfma_f32_16x16x32_f16 v[172:175], v[28:31], v[40:43], v[172:175]
	v_mfma_f32_16x16x32_f16 v[176:179], v[32:35], v[40:43], v[176:179]
	v_mfma_f32_16x16x32_f16 v[180:183], v[36:39], v[40:43], v[180:183]
	s_waitcnt lgkmcnt(2)
	v_mfma_f32_16x16x32_f16 v[184:187], v[16:19], v[44:47], v[184:187]
	v_mfma_f32_16x16x32_f16 v[188:191], v[20:23], v[44:47], v[188:191]
	v_mfma_f32_16x16x32_f16 v[192:195], v[24:27], v[44:47], v[192:195]
	v_mfma_f32_16x16x32_f16 v[196:199], v[28:31], v[44:47], v[196:199]
	v_mfma_f32_16x16x32_f16 v[200:203], v[32:35], v[44:47], v[200:203]
	v_mfma_f32_16x16x32_f16 v[204:207], v[36:39], v[44:47], v[204:207]
	s_waitcnt lgkmcnt(1)
	v_mfma_f32_16x16x32_f16 v[208:211], v[16:19], v[48:51], v[208:211]
	v_mfma_f32_16x16x32_f16 v[212:215], v[20:23], v[48:51], v[212:215]
	v_mfma_f32_16x16x32_f16 v[216:219], v[24:27], v[48:51], v[216:219]
	v_mfma_f32_16x16x32_f16 v[220:223], v[28:31], v[48:51], v[220:223]
	v_mfma_f32_16x16x32_f16 v[224:227], v[32:35], v[48:51], v[224:227]
	v_mfma_f32_16x16x32_f16 v[228:231], v[36:39], v[48:51], v[228:231]
	s_waitcnt lgkmcnt(0)
	v_mfma_f32_16x16x32_f16 v[232:235], v[16:19], v[52:55], v[232:235]
	v_mfma_f32_16x16x32_f16 v[236:239], v[20:23], v[52:55], v[236:239]
	v_mfma_f32_16x16x32_f16 v[240:243], v[24:27], v[52:55], v[240:243]
	v_mfma_f32_16x16x32_f16 v[244:247], v[28:31], v[52:55], v[244:247]
	v_mfma_f32_16x16x32_f16 v[248:251], v[32:35], v[52:55], v[248:251]
	v_mfma_f32_16x16x32_f16 v[252:255], v[36:39], v[52:55], v[252:255]
	ds_read_b128 v[16:19], v4 offset:40960
	ds_read_b128 v[20:23], v4 offset:41984
	ds_read_b128 v[24:27], v4 offset:43008
	ds_read_b128 v[28:31], v4 offset:44032
	ds_read_b128 v[32:35], v4 offset:45056
	ds_read_b128 v[36:39], v4 offset:46080
	ds_read_b128 v[40:43], v2 offset:40960
	ds_read_b128 v[44:47], v2 offset:41984
	ds_read_b128 v[48:51], v2 offset:43008
	ds_read_b128 v[52:55], v2 offset:44032
	s_cmp_eq_u32 s21, 11
	s_cbranch_scc1 .Lfc_ng_15
	s_add_u32 m0, s22, 0xa000
	s_nop 0
	global_load_lds_dwordx4 v5, s[26:27]
	s_add_u32 m0, s22, 0xa400
	s_nop 0
	global_load_lds_dwordx4 v6, s[26:27]
	s_add_u32 m0, s23, 0xa000
	s_nop 0
	global_load_lds_dwordx4 v11, s[30:31]
	s_add_u32 m0, s23, 0xa400
	s_nop 0
	global_load_lds_dwordx4 v11, s[34:35]
	s_add_u32 m0, s23, 0xa800
	s_nop 0
	global_load_lds_dwordx4 v11, s[38:39]
	s_add_u32 s26, s26, 0x80
	s_addc_u32 s27, s27, 0
	s_add_u32 s30, s30, 0x30000
	s_addc_u32 s31, s31, 0
	s_add_u32 s34, s34, 0x30000
	s_addc_u32 s35, s35, 0
	s_add_u32 s38, s38, 0x30000
	s_addc_u32 s39, s39, 0

.Lfc_w1_16:
	s_barrier
	s_waitcnt lgkmcnt(0)
	v_mfma_f32_16x16x32_f16 v[64:67], v[16:19], v[40:43], v[64:67]
	v_mfma_f32_16x16x32_f16 v[68:71], v[20:23], v[40:43], v[68:71]
	v_mfma_f32_16x16x32_f16 v[72:75], v[24:27], v[40:43], v[72:75]
	v_mfma_f32_16x16x32_f16 v[76:79], v[28:31], v[40:43], v[76:79]
	v_mfma_f32_16x16x32_f16 v[80:83], v[32:35], v[40:43], v[80:83]
	v_mfma_f32_16x16x32_f16 v[84:87], v[36:39], v[40:43], v[84:87]
	v_mfma_f32_16x16x32_f16 v[88:91], v[16:19], v[44:47], v[88:91]
	ds_read_b128 v[40:43], v2 offset:45056
	v_mfma_f32_16x16x32_f16 v[92:95], v[20:23], v[44:47], v[92:95]
	v_mfma_f32_16x16x32_f16 v[96:99], v[24:27], v[44:47], v[96:99]
	v_mfma_f32_16x16x32_f16 v[100:103], v[28:31], v[44:47], v[100:103]
	v_mfma_f32_16x16x32_f16 v[104:107], v[32:35], v[44:47], v[104:107]
	v_mfma_f32_16x16x32_f16 v[108:111], v[36:39], v[44:47], v[108:111]
	v_mfma_f32_16x16x32_f16 v[112:115], v[16:19], v[48:51], v[112:115]
	ds_read_b128 v[44:47], v2 offset:46080
	v_mfma_f32_16x16x32_f16 v[116:119], v[20:23], v[48:51], v[116:119]
	v_mfma_f32_16x16x32_f16 v[120:123], v[24:27], v[48:51], v[120:123]
	v_mfma_f32_16x16x32_f16 v[124:127], v[28:31], v[48:51], v[124:127]
	v_mfma_f32_16x16x32_f16 v[128:131], v[32:35], v[48:51], v[128:131]
	v_mfma_f32_16x16x32_f16 v[132:135], v[36:39], v[48:51], v[132:135]
	v_mfma_f32_16x16x32_f16 v[136:139], v[16:19], v[52:55], v[136:139]
	ds_read_b128 v[48:51], v2 offset:47104
	v_mfma_f32_16x16x32_f16 v[140:143], v[20:23], v[52:55], v[140:143]
	v_mfma_f32_16x16x32_f16 v[144:147], v[24:27], v[52:55], v[144:147]
	v_mfma_f32_16x16x32_f16 v[148:151], v[28:31], v[52:55], v[148:151]
	v_mfma_f32_16x16x32_f16 v[152:155], v[32:35], v[52:55], v[152:155]
	v_mfma_f32_16x16x32_f16 v[156:159], v[36:39], v[52:55], v[156:159]
	s_waitcnt lgkmcnt(2)
	v_mfma_f32_16x16x32_f16 v[160:163], v[16:19], v[40:43], v[160:163]
	ds_read_b128 v[52:55], v2 offset:48128
	v_mfma_f32_16x16x32_f16 v[164:167], v[20:23], v[40:43], v[164:167]
	v_mfma_f32_16x16x32_f16 v[168:171], v[24:27], v[40:43], v[168:171]
	v_mfma_f32_16x16x32_f16 v[172:175], v[28:31], v[40:43], v[172:175]
	v_mfma_f32_16x16x32_f16 v[176:179], v[32:35], v[40:43], v[176:179]
	v_mfma_f32_16x16x32_f16 v[180:183], v[36:39], v[40:43], v[180:183]
	s_waitcnt lgkmcnt(2)
	v_mfma_f32_16x16x32_f16 v[184:187], v[16:19], v[44:47], v[184:187]
	v_mfma_f32_16x16x32_f16 v[188:191], v[20:23], v[44:47], v[188:191]
	v_mfma_f32_16x16x32_f16 v[192:195], v[24:27], v[44:47], v[192:195]
	v_mfma_f32_16x16x32_f16 v[196:199], v[28:31], v[44:47], v[196:199]
	v_mfma_f32_16x16x32_f16 v[200:203], v[32:35], v[44:47], v[200:203]
	v_mfma_f32_16x16x32_f16 v[204:207], v[36:39], v[44:47], v[204:207]
	s_waitcnt lgkmcnt(1)
	v_mfma_f32_16x16x32_f16 v[208:211], v[16:19], v[48:51], v[208:211]
	v_mfma_f32_16x16x32_f16 v[212:215], v[20:23], v[48:51], v[212:215]
	v_mfma_f32_16x16x32_f16 v[216:219], v[24:27], v[48:51], v[216:219]
	v_mfma_f32_16x16x32_f16 v[220:223], v[28:31], v[48:51], v[220:223]
	v_mfma_f32_16x16x32_f16 v[224:227], v[32:35], v[48:51], v[224:227]
	v_mfma_f32_16x16x32_f16 v[228:231], v[36:39], v[48:51], v[228:231]
	s_waitcnt lgkmcnt(0)
	v_mfma_f32_16x16x32_f16 v[232:235], v[16:19], v[52:55], v[232:235]
	v_mfma_f32_16x16x32_f16 v[236:239], v[20:23], v[52:55], v[236:239]
	v_mfma_f32_16x16x32_f16 v[240:243], v[24:27], v[52:55], v[240:243]
	v_mfma_f32_16x16x32_f16 v[244:247], v[28:31], v[52:55], v[244:247]
	v_mfma_f32_16x16x32_f16 v[248:251], v[32:35], v[52:55], v[248:251]
	v_mfma_f32_16x16x32_f16 v[252:255], v[36:39], v[52:55], v[252:255]
	s_cmp_eq_u32 s21, 11
	s_cbranch_scc1 .Lfc_nr_17
	ds_read_b128 v[16:19], v3 offset:0
	ds_read_b128 v[20:23], v3 offset:1024
	ds_read_b128 v[24:27], v3 offset:2048
	ds_read_b128 v[28:31], v3 offset:3072
	ds_read_b128 v[32:35], v3 offset:4096
	ds_read_b128 v[36:39], v3 offset:5120
	ds_read_b128 v[40:43], v1 offset:0
	ds_read_b128 v[44:47], v1 offset:1024
	ds_read_b128 v[48:51], v1 offset:2048
	ds_read_b128 v[52:55], v1 offset:3072
	s_add_u32 m0, s22, 0x14000
	s_nop 0
	global_load_lds_dwordx4 v5, s[24:25]
	s_add_u32 m0, s22, 0x14400
	s_nop 0
	global_load_lds_dwordx4 v6, s[24:25]
	s_add_u32 m0, s23, 0x14000
	s_nop 0
	global_load_lds_dwordx4 v11, s[28:29]
	s_add_u32 m0, s23, 0x14400
	s_nop 0
	global_load_lds_dwordx4 v11, s[32:33]
	s_add_u32 m0, s23, 0x14800
	s_nop 0
	global_load_lds_dwordx4 v11, s[36:37]
	s_add_u32 s24, s24, 0x80
	s_addc_u32 s25, s25, 0
	s_add_u32 s28, s28, 0x30000
	s_addc_u32 s29, s29, 0
	s_add_u32 s32, s32, 0x30000
	s_addc_u32 s33, s33, 0
	s_add_u32 s36, s36, 0x30000
	s_addc_u32 s37, s37, 0

.Lfc_w1_18:
	s_barrier
	s_add_u32 s21, s21, 1
	s_cmp_lt_u32 s21, 12
	s_cbranch_scc1 .Lfc_h1_loop
